# static priority raise for waves 4-7 during the attention/mLSTM phases (reset at phase end)
# baseline (speedup 1.0000x reference)
.LBB0_392:
	s_andn2_b64 vcc, exec, s[0:1]
	v_readlane_b32 s0, v251, 53
	v_readlane_b32 s1, v251, 54
	s_nop 1
	v_cndmask_b32_e64 v1, 0, 1, s[0:1]
	v_cmp_ne_u32_e64 s[0:1], 1, v1
	s_nop 1
	v_writelane_b32 v252, s0, 59
	s_nop 1
	v_writelane_b32 v252, s1, 60
	s_cbranch_vccnz .LBB0_480
	v_readfirstlane_b32 s2, v0
	s_cmp_ge_u32 s2, 0x100
	s_cbranch_scc0 .LPR_a
	s_setprio 1
.LPR_a:
	v_readlane_b32 s0, v251, 4
	v_readlane_b32 s1, v251, 5
	s_load_dwordx8 s[4:11], s[0:1], 0x50
	s_waitcnt vmcnt(0)
	v_mov_b32_e32 v6, v0
	s_load_dwordx2 s[2:3], s[0:1], 0xc8
	s_waitcnt lgkmcnt(0)
	v_writelane_b32 v252, s4, 61
	s_nop 1
	v_writelane_b32 v253, s7, 0
	v_writelane_b32 v253, s8, 1
	v_writelane_b32 v253, s9, 2
	v_writelane_b32 v252, s5, 62
	v_writelane_b32 v253, s10, 3
	v_writelane_b32 v252, s6, 63
	v_writelane_b32 v253, s11, 4
	s_load_dwordx4 s[4:7], s[0:1], 0x70
	s_waitcnt lgkmcnt(0)
	v_writelane_b32 v253, s4, 5
	s_nop 1
	v_writelane_b32 v253, s5, 6
	v_writelane_b32 v253, s6, 7
	v_writelane_b32 v253, s7, 8
	v_readfirstlane_b32 s0, v6
	s_ashr_i32 s57, s0, 6
	v_and_b32_e32 v1, 63, v6
	v_writelane_b32 v253, s0, 9
	s_add_u32 s0, s2, 0x11400000
	v_writelane_b32 v253, s2, 10
	s_addc_u32 s1, s3, 0
	s_nop 0
	v_writelane_b32 v253, s3, 11
	v_writelane_b32 v253, s0, 12
	s_nop 1
	v_writelane_b32 v253, s1, 13
	v_readlane_b32 s0, v252, 59
	v_readlane_b32 s1, v252, 60
	s_and_b64 vcc, exec, s[0:1]
	s_cbranch_vccnz .LBB0_410
	v_readlane_b32 s4, v253, 10
	v_readlane_b32 s5, v253, 11
	s_add_u32 s0, s4, 0x200000
	s_addc_u32 s1, s5, 0
	v_writelane_b32 v253, s0, 14
	v_ashrrev_i32_e32 v3, 1, v6
	s_mov_b32 s13, s53
	v_writelane_b32 v253, s1, 15
	s_add_u32 s0, s4, 0x300000
	s_addc_u32 s1, s5, 0
	v_writelane_b32 v253, s0, 16
	v_and_b32_e32 v8, 1, v6
	v_lshlrev_b32_e32 v4, 7, v8
	v_writelane_b32 v253, s1, 17
	s_lshl_b32 s1, s57, 5
	v_readlane_b32 s0, v253, 9
	s_ashr_i32 s0, s0, 8
	s_and_b32 s1, s1, 0x60
	v_writelane_b32 v253, s1, 18
	s_lshl_b32 s1, s0, 7
	v_writelane_b32 v253, s1, 19
	s_lshl_b32 s0, s0, 6
	s_and_b32 s0, s0, 0xc0
	v_readlane_b32 s2, v253, 12
	v_readlane_b32 s3, v253, 13
	s_add_u32 s0, s2, s0
	v_writelane_b32 v253, s0, 20
	s_addc_u32 s0, s3, 0
	v_writelane_b32 v253, s0, 21
	s_add_u32 s0, s4, 0xd400000
	s_addc_u32 s1, s5, 0
	v_writelane_b32 v253, s0, 22
	s_lshl_b32 s52, s46, 3
	v_readlane_b32 s4, v252, 61
	v_writelane_b32 v253, s1, 23
	s_lshl_b32 s12, s46, 6
	s_lshl_b64 s[0:1], s[52:53], 2
	v_readlane_b32 s8, v253, 1
	v_readlane_b32 s9, v253, 2
	s_add_u32 s0, s8, s0
	s_addc_u32 s1, s9, s1
	v_readlane_b32 s7, v253, 0
	v_readlane_b32 s10, v253, 3
	v_readlane_b32 s11, v253, 4
	v_writelane_b32 v253, s0, 24
	v_readlane_b32 s6, v252, 63
	v_mov_b32_e32 v5, v2
	v_writelane_b32 v253, s1, 25
	s_movk_i32 s0, 0x7f
	v_cmp_lt_i32_e64 s[0:1], s0, v3
	v_add_u32_e32 v7, 0xffffff80, v3
	v_lshlrev_b32_e32 v132, 5, v8
	v_writelane_b32 v253, s0, 26
	v_mov_b32_e32 v133, v2
	v_readlane_b32 s5, v252, 62
	v_writelane_b32 v253, s1, 27
	s_mov_b32 s0, s12
	v_writelane_b32 v253, s0, 28
	s_nop 1
	v_writelane_b32 v253, s1, 29
	s_lshl_b64 s[0:1], s[12:13], 2
	s_add_u32 s0, s6, s0
	s_addc_u32 s1, s7, s1
	v_lshl_add_u64 v[134:135], s[0:1], 0, v[4:5]
	v_cmp_eq_u32_e64 s[0:1], 0, v8
	s_nop 1
	v_writelane_b32 v253, s0, 30
	s_nop 1
	v_writelane_b32 v253, s1, 31
	s_movk_i32 s0, 0x90
	v_mul_lo_u32 v4, v3, s0
	v_add_u32_e32 v4, 0, v4
	s_movk_i32 s0, 0xff72
	v_lshl_add_u32 v170, v8, 6, v4
	v_mad_u64_u32 v[4:5], s[0:1], v3, s0, v[4:5]
	v_cmp_gt_i32_e64 s[0:1], 64, v6
	v_mul_u32_u24_e32 v3, 0x4600, v8
	v_add_u32_e32 v174, v4, v3
	v_writelane_b32 v253, s0, 32
	s_nop 1
	v_writelane_b32 v253, s1, 33
	s_movk_i32 s0, 0x230
	v_mul_lo_u32 v5, v6, s0
	s_and_b32 s0, s57, 3
	s_lshl_b32 s1, s0, 5
	s_or_b32 s4, s1, 16
	v_writelane_b32 v253, s4, 34
	s_add_i32 s4, s1, 32
	v_writelane_b32 v253, s4, 35
	s_add_i32 s4, s1, 48
	v_writelane_b32 v253, s4, 36
	s_add_i32 s4, s1, 64
	v_writelane_b32 v253, s4, 37
	s_add_i32 s4, s1, 0x50
	v_writelane_b32 v253, s4, 38
	s_add_i32 s4, s1, 0x60
	v_writelane_b32 v253, s4, 39
	v_writelane_b32 v253, s1, 40
	s_addk_i32 s1, 0x70
	v_writelane_b32 v253, s1, 41
	s_add_i32 s1, s57, 8
	s_ashr_i32 s1, s1, 2
	v_writelane_b32 v253, s1, 42
	s_lshl_b32 s1, s1, 6
	s_and_b32 s1, s1, 0xc0
	s_add_u32 s1, s2, s1
	v_writelane_b32 v253, s1, 43
	s_addc_u32 s1, s3, 0
	s_lshl_b32 s0, s0, 6
	v_writelane_b32 v253, s1, 44
	s_add_i32 s0, s0, 0
	v_writelane_b32 v253, s0, 45
	v_add_u32_e32 v175, 0, v5
	v_readlane_b32 s0, v251, 0
	v_readlane_b32 s1, v251, 1
	s_branch .LBB0_396

.LBB0_433:
	s_setprio 0
	v_readlane_b32 s46, v252, 58
	s_mul_i32 s0, s46, 10
	s_add_i32 s30, s0, 4
	v_readlane_b32 s0, v251, 10
	v_readlane_b32 s3, v251, 13
	s_cmp_lt_i32 s30, s3
	v_readlane_b32 s1, v251, 11
	v_readlane_b32 s2, v251, 12
	s_cbranch_scc0 .LBB0_446
	s_waitcnt vmcnt(0)
	s_waitcnt vmcnt(0)
	s_barrier
	s_mov_b64 s[0:1], exec
	v_readlane_b32 s2, v252, 42
	v_readlane_b32 s3, v252, 43
	s_and_b64 s[2:3], s[0:1], s[2:3]
	v_readlane_b32 s47, v252, 56
	s_mov_b32 s53, s37
	s_mov_b64 exec, s[2:3]
	s_cbranch_execz .LBB0_479
	v_readlane_b32 s2, v251, 8
	v_readlane_b32 s4, v252, 19
	v_readlane_b32 s3, v251, 9
	s_waitcnt vmcnt(0) expcnt(0) lgkmcnt(0)
	v_mov_b32_e32 v1, s4
	ds_read_b32 v6, v1
	v_readlane_b32 s4, v252, 20
	s_waitcnt lgkmcnt(0)
	v_cmp_ne_u32_e32 vcc, 0, v6
	v_mov_b32_e32 v1, s4
	ds_read_b32 v4, v1
	s_cbranch_vccnz .LBB0_450
	v_readlane_b32 s4, v251, 6
	v_readlane_b32 s5, v251, 7
	s_load_dwordx2 s[8:9], s[4:5], 0x4
	s_add_u32 s4, s2, 0x1000
	s_addc_u32 s5, s3, 0
	s_add_u32 s6, s2, 0x1100
	s_addc_u32 s7, s3, 0
	v_readlane_b32 s10, v251, 2
	s_waitcnt lgkmcnt(0)
	s_mul_i32 s31, s8, s10
	s_add_u32 s8, s2, 0x1200
	s_mul_i32 s31, s31, s9
	s_addc_u32 s9, s3, 0
	v_readlane_b32 s11, v251, 3
	s_add_u32 s10, s2, 0x1300
	s_addc_u32 s11, s3, 0
	s_mov_b32 s33, 1
	s_mov_b64 s[12:13], 0
	s_branch .LBB0_439

.LBB0_534:
	s_andn2_b64 vcc, exec, s[0:1]
	s_cbranch_vccnz .LBB0_607
	v_readfirstlane_b32 s6, v0
	s_cmp_ge_u32 s6, 0x100
	s_cbranch_scc0 .LPR_b
	s_setprio 1
.LPR_b:
	v_readlane_b32 s4, v251, 4
	v_readlane_b32 s0, v251, 55
	v_readlane_b32 s5, v251, 5
	s_waitcnt vmcnt(0)
	v_mov_b32_e32 v4, v0
	v_readlane_b32 s1, v251, 56
	s_and_b64 vcc, exec, s[0:1]
	v_readfirstlane_b32 s6, v4
	s_cbranch_vccz .LBB0_560
	s_load_dwordx4 s[0:3], s[4:5], 0x68
	s_load_dwordx2 s[10:11], s[4:5], 0x78
	s_nop 0
	s_load_dwordx2 s[4:5], s[4:5], 0xc8
	s_ashr_i32 s7, s6, 6
	s_lshl_b32 s14, s46, 2
	s_lshl_b32 s8, s46, 10
	v_min_i32_e32 v3, 0x4ff, v4
	s_waitcnt lgkmcnt(0)
	s_add_u32 s24, s4, 0x11400000
	s_addc_u32 s25, s5, 0
	s_add_u32 s26, s4, 0xe400000
	s_addc_u32 s27, s5, 0
	s_add_u32 s12, s4, 0x400000
	s_addc_u32 s13, s5, 0
	v_ashrrev_i32_e32 v5, 8, v3
	s_mov_b32 s9, s53
	s_add_u32 s28, s4, 0x24600000
	v_add_u32_e32 v6, s14, v5
	s_addc_u32 s29, s5, 0
	s_lshl_b64 s[8:9], s[8:9], 2
	v_ashrrev_i32_e32 v7, 31, v6
	s_add_u32 s2, s2, s8
	v_lshlrev_b64 v[6:7], 12, v[6:7]
	s_addc_u32 s3, s3, s9
	v_lshl_add_u64 v[6:7], s[0:1], 0, v[6:7]
	v_cmp_gt_i32_e32 vcc, 4, v5
	v_mov_b32_e32 v5, s2
	s_waitcnt vmcnt(0)
	v_mov_b32_e32 v8, s3
	v_cndmask_b32_e32 v76, v5, v6, vcc
	v_min_i32_e32 v6, 0x2ff, v4
	v_cndmask_b32_e32 v77, v8, v7, vcc
	v_add_u32_e32 v7, 0x200, v6
	v_ashrrev_i32_e32 v9, 8, v7
	v_and_b32_e32 v106, 0xff, v6
	v_add_u32_e32 v6, s14, v9
	v_ashrrev_i32_e32 v7, 31, v6
	v_lshlrev_b64 v[6:7], 12, v[6:7]
	v_lshl_add_u64 v[6:7], s[0:1], 0, v[6:7]
	v_cmp_gt_i32_e32 vcc, 4, v9
	s_movk_i32 s8, 0x80
	v_lshlrev_b32_e32 v113, 1, v4
	v_cndmask_b32_e32 v78, v5, v6, vcc
	v_min_i32_e32 v6, 0xff, v4
	v_cndmask_b32_e32 v79, v8, v7, vcc
	v_add_u32_e32 v7, 0x400, v6
	v_ashrrev_i32_e32 v9, 8, v7
	v_and_b32_e32 v107, 0xff, v6
	v_add_u32_e32 v6, s14, v9
	v_ashrrev_i32_e32 v7, 31, v6
	v_lshlrev_b64 v[6:7], 12, v[6:7]
	v_lshl_add_u64 v[6:7], s[0:1], 0, v[6:7]
	v_cmp_gt_i32_e32 vcc, 4, v9
	v_readlane_b32 s0, v252, 21
	v_cmp_gt_u32_e64 s[2:3], s8, v107
	v_cndmask_b32_e32 v80, v5, v6, vcc
	v_and_b32_e32 v5, 0x7f, v4
	v_lshl_or_b32 v108, s46, 9, v5
	v_lshlrev_b32_e32 v5, 2, v4
	v_add_u32_e32 v109, s0, v5
	s_movk_i32 s0, 0x100
	v_cmp_gt_i32_e64 s[48:49], s0, v4
	v_readlane_b32 s0, v252, 22
	v_writelane_b32 v253, s2, 47
	v_cndmask_b32_e32 v81, v8, v7, vcc
	v_add_u32_e32 v110, s0, v5
	s_movk_i32 s0, 0x480
	v_cmp_gt_i32_e64 s[54:55], s0, v4
	s_lshl_b32 s0, s7, 4
	s_ashr_i32 s1, s0, 31
	v_max_i32_e32 v5, 0x280, v4
	v_writelane_b32 v253, s3, 48
	s_lshl_b64 s[2:3], s[0:1], 1
	v_sub_u32_e32 v5, v5, v4
	s_add_u32 s1, s4, s2
	v_add_u32_e32 v5, 0x1ff, v5
	s_addc_u32 s2, s5, s3
	v_lshrrev_b32_e32 v6, 9, v5
	s_movk_i32 s4, 0x5ff
	s_add_u32 s1, s1, 0xa00000
	v_add_u32_e32 v9, 1, v6
	v_cmp_lt_u32_e64 s[4:5], s4, v5
	s_addc_u32 s30, s2, 0
	s_lshl_b32 s2, s7, 5
	v_writelane_b32 v253, s4, 49
	v_and_b32_e32 v111, 0xfffffc, v9
	s_add_i32 s31, s2, 0
	v_writelane_b32 v253, s5, 50
	v_cmp_ne_u32_e64 s[4:5], v9, v111
	s_add_i32 s31, s31, 0x12100
	v_lshlrev_b32_e32 v8, 3, v4
	v_writelane_b32 v253, s4, 51
	s_cmp_lt_u32 s6, 64
	v_and_b32_e32 v3, 0xff, v3
	v_writelane_b32 v253, s5, 52
	v_readlane_b32 s4, v252, 30
	s_cselect_b64 s[2:3], -1, 0
	s_and_b32 s14, s0, 0xffffffc0
	s_or_b32 s16, s0, 48
	v_add_u32_e32 v114, s4, v113
	v_add_u32_e32 v8, 0, v8
	v_readlane_b32 s4, v251, 0
	v_and_b32_e32 v1, 63, v4
	v_cmp_gt_u32_e64 s[42:43], s8, v3
	v_cmp_gt_u32_e64 s[44:45], s8, v106
	v_cmp_gt_i32_e64 s[50:51], s8, v4
	s_and_b32 s34, s0, 48
	s_and_b32 s35, s6, 0xffffff00
	s_ashr_i32 s15, s14, 31
	s_or_b32 s36, s14, 16
	s_or_b32 s37, s14, 32
	s_ashr_i32 s17, s16, 31
	v_lshl_add_u32 v112, v111, 9, v4
	v_add_u32_e32 v7, 0x600, v4
	v_add_u32_e32 v6, 0x400, v4
	v_add_u32_e32 v5, 0x200, v4
	v_add_u32_e32 v115, 0x1d400, v8
	v_readlane_b32 s38, v251, 57
	v_readlane_b32 s39, v251, 58
	s_mov_b32 s40, s4
	v_readlane_b32 s5, v251, 1
	s_branch .LBB0_538

.LBB0_560:
	s_setprio 0
	s_mul_i32 s0, s46, 10
	s_add_i32 s30, s0, 6
	v_readlane_b32 s0, v251, 10
	v_readlane_b32 s3, v251, 13
	s_cmp_lt_i32 s30, s3
	v_readlane_b32 s1, v251, 11
	v_readlane_b32 s2, v251, 12
	s_cbranch_scc0 .LBB0_573
	s_waitcnt vmcnt(0)
	s_waitcnt vmcnt(0) lgkmcnt(0)
	s_barrier
	s_mov_b64 s[0:1], exec
	v_readlane_b32 s2, v252, 42
	v_readlane_b32 s3, v252, 43
	s_and_b64 s[2:3], s[0:1], s[2:3]
	v_readlane_b32 s47, v252, 56
	s_mov_b64 exec, s[2:3]
	s_cbranch_execz .LBB0_606
	v_readlane_b32 s2, v251, 8
	v_readlane_b32 s4, v252, 19
	v_readlane_b32 s3, v251, 9
	s_waitcnt vmcnt(0) expcnt(0) lgkmcnt(0)
	v_mov_b32_e32 v1, s4
	ds_read_b32 v6, v1
	v_readlane_b32 s4, v252, 20
	s_waitcnt lgkmcnt(0)
	v_cmp_ne_u32_e32 vcc, 0, v6
	v_mov_b32_e32 v1, s4
	ds_read_b32 v4, v1
	s_cbranch_vccnz .LBB0_577
	v_readlane_b32 s4, v251, 6
	v_readlane_b32 s5, v251, 7
	s_load_dwordx2 s[8:9], s[4:5], 0x4
	s_add_u32 s4, s2, 0x1000
	s_addc_u32 s5, s3, 0
	s_add_u32 s6, s2, 0x1100
	s_addc_u32 s7, s3, 0
	v_readlane_b32 s10, v251, 2
	s_waitcnt lgkmcnt(0)
	s_mul_i32 s31, s8, s10
	s_add_u32 s8, s2, 0x1200
	s_mul_i32 s31, s31, s9
	s_addc_u32 s9, s3, 0
	v_readlane_b32 s11, v251, 3
	s_add_u32 s10, s2, 0x1300
	s_addc_u32 s11, s3, 0
	s_mov_b32 s33, 1
	s_mov_b64 s[12:13], 0
	s_branch .LBB0_566
